# prologue modulation GEMV: 8 serial rounds of 16 weight-row loads replaced by one 128-load burst into spare VGPRs, copied out per trip
# baseline (speedup 1.0000x reference)
; #define LAS __attribute__((address_space(3)))
; __global__ void __launch_bounds__(NTHR, 2) mk_fwd(Args args) {
;     ...
;         for (int t = bx; t < 192; t += G) {
;             LAS float* red = (LAS float*)lds;
;             const LAS float* sl = (const LAS float*)lds + 8704;
;             const int l = t / 96, nb = t % 96, n = nb * 64 + lane;
;             float acc[17];
; #pragma unroll
;             for (int r = 0; r < 17; ++r) acc[r] = 0.f;
;             const float* W = w_mod + (size_t)l * DM * (NMOD * DM) + n;
; #pragma unroll 1
;             for (int k0 = wave * 128; k0 < wave * 128 + 128; k0 += 16) {
;                 float wv[16];
; #pragma unroll
;                 for (int i = 0; i < 16; ++i) wv[i] = W[(size_t)(k0 + i) * (NMOD * DM)];
.LBB0_16:
	s_mul_hi_i32 s4, s63, 0x2aaaaaab
	s_lshr_b32 s5, s4, 31
	s_ashr_i32 s4, s4, 4
	s_add_i32 s11, s4, s5
	s_mul_i32 s4, s11, 0x60
	s_sub_i32 s4, s63, s4
	s_lshl_b32 s10, s4, 6
	s_mul_i32 s4, s11, 0x1800000
	v_or_b32_e32 v2, s10, v1
	s_mul_hi_i32 s5, s11, 0x1800000
	s_add_u32 s4, s45, s4
	v_ashrrev_i32_e32 v3, 31, v2
	s_addc_u32 s5, s46, s5
	v_lshl_add_u64 v[80:81], v[2:3], 2, s[4:5]
	s_mov_b32 s26, s47
	s_mov_b32 s27, s35
	v_mov_b32_e32 v109, 0
	v_mov_b32_e32 v2, 0
	v_mov_b32_e32 v3, v77
	v_mov_b32_e32 v10, 0
	v_mov_b32_e32 v11, v77
	v_mov_b32_e32 v18, 0
	v_mov_b32_e32 v19, v77
	v_mov_b32_e32 v34, 0
	v_mov_b32_e32 v35, v77
	v_mov_b32_e32 v92, 0
	v_mov_b32_e32 v93, v77
	v_mov_b32_e32 v96, 0
	v_mov_b32_e32 v97, v77
	v_mov_b32_e32 v98, 0
	v_mov_b32_e32 v99, v77
	v_mov_b32_e32 v94, 0
	v_mov_b32_e32 v95, v77
	s_mov_b32 s98, 0
	v_mov_b32_e32 v6, v80
	v_mov_b32_e32 v7, v81
	global_load_dword v128, v[6:7], off
	v_add_co_u32_e64 v4, s[4:5], s44, v6
	s_nop 1
	v_addc_co_u32_e64 v5, s[4:5], 0, v7, s[4:5]
	global_load_dword v129, v[4:5], off
	v_add_co_u32_e64 v4, s[4:5], s48, v6
	s_nop 1
	v_addc_co_u32_e64 v5, s[4:5], 0, v7, s[4:5]
	global_load_dword v130, v[4:5], off
	v_add_co_u32_e64 v4, s[4:5], s49, v6
	s_nop 1
	v_addc_co_u32_e64 v5, s[4:5], 0, v7, s[4:5]
	global_load_dword v131, v[4:5], off
	v_add_co_u32_e64 v4, s[4:5], s50, v6
	s_nop 1
	v_addc_co_u32_e64 v5, s[4:5], 0, v7, s[4:5]
	global_load_dword v132, v[4:5], off
	v_add_co_u32_e64 v4, s[4:5], s51, v6
	s_nop 1
	v_addc_co_u32_e64 v5, s[4:5], 0, v7, s[4:5]
	global_load_dword v133, v[4:5], off
	v_add_co_u32_e64 v4, s[4:5], s52, v6
	s_nop 1
	v_addc_co_u32_e64 v5, s[4:5], 0, v7, s[4:5]
	global_load_dword v134, v[4:5], off
	v_add_co_u32_e64 v4, s[4:5], s53, v6
	s_nop 1
	v_addc_co_u32_e64 v5, s[4:5], 0, v7, s[4:5]
	global_load_dword v135, v[4:5], off
	v_add_co_u32_e64 v4, s[4:5], s54, v6
	s_nop 1
	v_addc_co_u32_e64 v5, s[4:5], 0, v7, s[4:5]
	global_load_dword v136, v[4:5], off
	v_add_co_u32_e64 v4, s[4:5], s55, v6
	s_nop 1
	v_addc_co_u32_e64 v5, s[4:5], 0, v7, s[4:5]
	global_load_dword v137, v[4:5], off
	v_add_co_u32_e64 v4, s[4:5], s56, v6
	s_nop 1
	v_addc_co_u32_e64 v5, s[4:5], 0, v7, s[4:5]
	global_load_dword v138, v[4:5], off
	v_add_co_u32_e64 v4, s[4:5], s57, v6
	s_nop 1
	v_addc_co_u32_e64 v5, s[4:5], 0, v7, s[4:5]
	global_load_dword v139, v[4:5], off
	v_add_co_u32_e64 v4, s[4:5], s58, v6
	s_nop 1
	v_addc_co_u32_e64 v5, s[4:5], 0, v7, s[4:5]
	global_load_dword v140, v[4:5], off
	v_add_co_u32_e64 v4, s[4:5], s59, v6
	s_nop 1
	v_addc_co_u32_e64 v5, s[4:5], 0, v7, s[4:5]
	global_load_dword v141, v[4:5], off
	v_add_co_u32_e64 v4, s[4:5], s60, v6
	s_nop 1
	v_addc_co_u32_e64 v5, s[4:5], 0, v7, s[4:5]
	global_load_dword v142, v[4:5], off
	v_add_co_u32_e64 v4, s[4:5], s61, v6
	s_nop 1
	v_addc_co_u32_e64 v5, s[4:5], 0, v7, s[4:5]
	global_load_dword v143, v[4:5], off
	v_lshl_add_u64 v[6:7], v[6:7], 0, s[6:7]
	global_load_dword v144, v[6:7], off
	v_add_co_u32_e64 v4, s[4:5], s44, v6
	s_nop 1
	v_addc_co_u32_e64 v5, s[4:5], 0, v7, s[4:5]
	global_load_dword v145, v[4:5], off
	v_add_co_u32_e64 v4, s[4:5], s48, v6
	s_nop 1
	v_addc_co_u32_e64 v5, s[4:5], 0, v7, s[4:5]
	global_load_dword v146, v[4:5], off
	v_add_co_u32_e64 v4, s[4:5], s49, v6
	s_nop 1
	v_addc_co_u32_e64 v5, s[4:5], 0, v7, s[4:5]
	global_load_dword v147, v[4:5], off
	v_add_co_u32_e64 v4, s[4:5], s50, v6
	s_nop 1
	v_addc_co_u32_e64 v5, s[4:5], 0, v7, s[4:5]
	global_load_dword v148, v[4:5], off
	v_add_co_u32_e64 v4, s[4:5], s51, v6
	s_nop 1
	v_addc_co_u32_e64 v5, s[4:5], 0, v7, s[4:5]
	global_load_dword v149, v[4:5], off
	v_add_co_u32_e64 v4, s[4:5], s52, v6
	s_nop 1
	v_addc_co_u32_e64 v5, s[4:5], 0, v7, s[4:5]
	global_load_dword v150, v[4:5], off
	v_add_co_u32_e64 v4, s[4:5], s53, v6
	s_nop 1
	v_addc_co_u32_e64 v5, s[4:5], 0, v7, s[4:5]
	global_load_dword v151, v[4:5], off
	v_add_co_u32_e64 v4, s[4:5], s54, v6
	s_nop 1
	v_addc_co_u32_e64 v5, s[4:5], 0, v7, s[4:5]
	global_load_dword v152, v[4:5], off
	v_add_co_u32_e64 v4, s[4:5], s55, v6
	s_nop 1
	v_addc_co_u32_e64 v5, s[4:5], 0, v7, s[4:5]
	global_load_dword v153, v[4:5], off
	v_add_co_u32_e64 v4, s[4:5], s56, v6
	s_nop 1
	v_addc_co_u32_e64 v5, s[4:5], 0, v7, s[4:5]
	global_load_dword v154, v[4:5], off
	v_add_co_u32_e64 v4, s[4:5], s57, v6
	s_nop 1
	v_addc_co_u32_e64 v5, s[4:5], 0, v7, s[4:5]
	global_load_dword v155, v[4:5], off
	v_add_co_u32_e64 v4, s[4:5], s58, v6
	s_nop 1
	v_addc_co_u32_e64 v5, s[4:5], 0, v7, s[4:5]
	global_load_dword v156, v[4:5], off
	v_add_co_u32_e64 v4, s[4:5], s59, v6
	s_nop 1
	v_addc_co_u32_e64 v5, s[4:5], 0, v7, s[4:5]
	global_load_dword v157, v[4:5], off
	v_add_co_u32_e64 v4, s[4:5], s60, v6
	s_nop 1
	v_addc_co_u32_e64 v5, s[4:5], 0, v7, s[4:5]
	global_load_dword v158, v[4:5], off
	v_add_co_u32_e64 v4, s[4:5], s61, v6
	s_nop 1
	v_addc_co_u32_e64 v5, s[4:5], 0, v7, s[4:5]
	global_load_dword v159, v[4:5], off
	v_lshl_add_u64 v[6:7], v[6:7], 0, s[6:7]
	global_load_dword v160, v[6:7], off
	v_add_co_u32_e64 v4, s[4:5], s44, v6
	s_nop 1
	v_addc_co_u32_e64 v5, s[4:5], 0, v7, s[4:5]
	global_load_dword v161, v[4:5], off
	v_add_co_u32_e64 v4, s[4:5], s48, v6
	s_nop 1
	v_addc_co_u32_e64 v5, s[4:5], 0, v7, s[4:5]
	global_load_dword v162, v[4:5], off
	v_add_co_u32_e64 v4, s[4:5], s49, v6
	s_nop 1
	v_addc_co_u32_e64 v5, s[4:5], 0, v7, s[4:5]
	global_load_dword v163, v[4:5], off
	v_add_co_u32_e64 v4, s[4:5], s50, v6
	s_nop 1
	v_addc_co_u32_e64 v5, s[4:5], 0, v7, s[4:5]
	global_load_dword v164, v[4:5], off
	v_add_co_u32_e64 v4, s[4:5], s51, v6
	s_nop 1
	v_addc_co_u32_e64 v5, s[4:5], 0, v7, s[4:5]
	global_load_dword v165, v[4:5], off
	v_add_co_u32_e64 v4, s[4:5], s52, v6
	s_nop 1
; __global__ void __launch_bounds__(NTHR, 2) mk_fwd(Args args) {
;     ...
;             for (int k0 = wave * 128; k0 < wave * 128 + 128; k0 += 16) {
;                 float wv[16];
; #pragma unroll
;                 for (int i = 0; i < 16; ++i) wv[i] = W[(size_t)(k0 + i) * (NMOD * DM)];
	v_addc_co_u32_e64 v5, s[4:5], 0, v7, s[4:5]
	global_load_dword v166, v[4:5], off
	v_add_co_u32_e64 v4, s[4:5], s53, v6
	s_nop 1
	v_addc_co_u32_e64 v5, s[4:5], 0, v7, s[4:5]
	global_load_dword v167, v[4:5], off
	v_add_co_u32_e64 v4, s[4:5], s54, v6
	s_nop 1
	v_addc_co_u32_e64 v5, s[4:5], 0, v7, s[4:5]
	global_load_dword v168, v[4:5], off
	v_add_co_u32_e64 v4, s[4:5], s55, v6
	s_nop 1
	v_addc_co_u32_e64 v5, s[4:5], 0, v7, s[4:5]
	global_load_dword v169, v[4:5], off
	v_add_co_u32_e64 v4, s[4:5], s56, v6
	s_nop 1
	v_addc_co_u32_e64 v5, s[4:5], 0, v7, s[4:5]
	global_load_dword v170, v[4:5], off
	v_add_co_u32_e64 v4, s[4:5], s57, v6
	s_nop 1
	v_addc_co_u32_e64 v5, s[4:5], 0, v7, s[4:5]
	global_load_dword v171, v[4:5], off
	v_add_co_u32_e64 v4, s[4:5], s58, v6
	s_nop 1
	v_addc_co_u32_e64 v5, s[4:5], 0, v7, s[4:5]
	global_load_dword v172, v[4:5], off
	v_add_co_u32_e64 v4, s[4:5], s59, v6
	s_nop 1
	v_addc_co_u32_e64 v5, s[4:5], 0, v7, s[4:5]
	global_load_dword v173, v[4:5], off
	v_add_co_u32_e64 v4, s[4:5], s60, v6
	s_nop 1
	v_addc_co_u32_e64 v5, s[4:5], 0, v7, s[4:5]
	global_load_dword v174, v[4:5], off
	v_add_co_u32_e64 v4, s[4:5], s61, v6
	s_nop 1
	v_addc_co_u32_e64 v5, s[4:5], 0, v7, s[4:5]
	global_load_dword v175, v[4:5], off
	v_lshl_add_u64 v[6:7], v[6:7], 0, s[6:7]
	global_load_dword v176, v[6:7], off
	v_add_co_u32_e64 v4, s[4:5], s44, v6
	s_nop 1
	v_addc_co_u32_e64 v5, s[4:5], 0, v7, s[4:5]
	global_load_dword v177, v[4:5], off
	v_add_co_u32_e64 v4, s[4:5], s48, v6
	s_nop 1
	v_addc_co_u32_e64 v5, s[4:5], 0, v7, s[4:5]
	global_load_dword v178, v[4:5], off
	v_add_co_u32_e64 v4, s[4:5], s49, v6
	s_nop 1
	v_addc_co_u32_e64 v5, s[4:5], 0, v7, s[4:5]
	global_load_dword v179, v[4:5], off
	v_add_co_u32_e64 v4, s[4:5], s50, v6
	s_nop 1
	v_addc_co_u32_e64 v5, s[4:5], 0, v7, s[4:5]
	global_load_dword v180, v[4:5], off
	v_add_co_u32_e64 v4, s[4:5], s51, v6
	s_nop 1
	v_addc_co_u32_e64 v5, s[4:5], 0, v7, s[4:5]
	global_load_dword v181, v[4:5], off
	v_add_co_u32_e64 v4, s[4:5], s52, v6
	s_nop 1
	v_addc_co_u32_e64 v5, s[4:5], 0, v7, s[4:5]
	global_load_dword v182, v[4:5], off
	v_add_co_u32_e64 v4, s[4:5], s53, v6
	s_nop 1
	v_addc_co_u32_e64 v5, s[4:5], 0, v7, s[4:5]
	global_load_dword v183, v[4:5], off
	v_add_co_u32_e64 v4, s[4:5], s54, v6
	s_nop 1
	v_addc_co_u32_e64 v5, s[4:5], 0, v7, s[4:5]
	global_load_dword v184, v[4:5], off
	v_add_co_u32_e64 v4, s[4:5], s55, v6
	s_nop 1
	v_addc_co_u32_e64 v5, s[4:5], 0, v7, s[4:5]
	global_load_dword v185, v[4:5], off
	v_add_co_u32_e64 v4, s[4:5], s56, v6
	s_nop 1
	v_addc_co_u32_e64 v5, s[4:5], 0, v7, s[4:5]
	global_load_dword v186, v[4:5], off
	v_add_co_u32_e64 v4, s[4:5], s57, v6
	s_nop 1
	v_addc_co_u32_e64 v5, s[4:5], 0, v7, s[4:5]
	global_load_dword v187, v[4:5], off
	v_add_co_u32_e64 v4, s[4:5], s58, v6
	s_nop 1
	v_addc_co_u32_e64 v5, s[4:5], 0, v7, s[4:5]
	global_load_dword v188, v[4:5], off
	v_add_co_u32_e64 v4, s[4:5], s59, v6
	s_nop 1
	v_addc_co_u32_e64 v5, s[4:5], 0, v7, s[4:5]
	global_load_dword v189, v[4:5], off
	v_add_co_u32_e64 v4, s[4:5], s60, v6
	s_nop 1
	v_addc_co_u32_e64 v5, s[4:5], 0, v7, s[4:5]
	global_load_dword v190, v[4:5], off
	v_add_co_u32_e64 v4, s[4:5], s61, v6
	s_nop 1
	v_addc_co_u32_e64 v5, s[4:5], 0, v7, s[4:5]
	global_load_dword v191, v[4:5], off
	v_lshl_add_u64 v[6:7], v[6:7], 0, s[6:7]
	global_load_dword v192, v[6:7], off
	v_add_co_u32_e64 v4, s[4:5], s44, v6
	s_nop 1
	v_addc_co_u32_e64 v5, s[4:5], 0, v7, s[4:5]
	global_load_dword v193, v[4:5], off
	v_add_co_u32_e64 v4, s[4:5], s48, v6
	s_nop 1
	v_addc_co_u32_e64 v5, s[4:5], 0, v7, s[4:5]
	global_load_dword v194, v[4:5], off
	v_add_co_u32_e64 v4, s[4:5], s49, v6
	s_nop 1
	v_addc_co_u32_e64 v5, s[4:5], 0, v7, s[4:5]
	global_load_dword v195, v[4:5], off
	v_add_co_u32_e64 v4, s[4:5], s50, v6
	s_nop 1
	v_addc_co_u32_e64 v5, s[4:5], 0, v7, s[4:5]
	global_load_dword v196, v[4:5], off
	v_add_co_u32_e64 v4, s[4:5], s51, v6
	s_nop 1
	v_addc_co_u32_e64 v5, s[4:5], 0, v7, s[4:5]
	global_load_dword v197, v[4:5], off
	v_add_co_u32_e64 v4, s[4:5], s52, v6
	s_nop 1
	v_addc_co_u32_e64 v5, s[4:5], 0, v7, s[4:5]
	global_load_dword v198, v[4:5], off
	v_add_co_u32_e64 v4, s[4:5], s53, v6
	s_nop 1
	v_addc_co_u32_e64 v5, s[4:5], 0, v7, s[4:5]
	global_load_dword v199, v[4:5], off
	v_add_co_u32_e64 v4, s[4:5], s54, v6
	s_nop 1
	v_addc_co_u32_e64 v5, s[4:5], 0, v7, s[4:5]
	global_load_dword v200, v[4:5], off
	v_add_co_u32_e64 v4, s[4:5], s55, v6
	s_nop 1
	v_addc_co_u32_e64 v5, s[4:5], 0, v7, s[4:5]
	global_load_dword v201, v[4:5], off
	v_add_co_u32_e64 v4, s[4:5], s56, v6
	s_nop 1
	v_addc_co_u32_e64 v5, s[4:5], 0, v7, s[4:5]
	global_load_dword v202, v[4:5], off
	v_add_co_u32_e64 v4, s[4:5], s57, v6
	s_nop 1
	v_addc_co_u32_e64 v5, s[4:5], 0, v7, s[4:5]
	global_load_dword v203, v[4:5], off
	v_add_co_u32_e64 v4, s[4:5], s58, v6
	s_nop 1
	v_addc_co_u32_e64 v5, s[4:5], 0, v7, s[4:5]
	global_load_dword v204, v[4:5], off
	v_add_co_u32_e64 v4, s[4:5], s59, v6
	s_nop 1
	v_addc_co_u32_e64 v5, s[4:5], 0, v7, s[4:5]
	global_load_dword v205, v[4:5], off
	v_add_co_u32_e64 v4, s[4:5], s60, v6
	s_nop 1
	v_addc_co_u32_e64 v5, s[4:5], 0, v7, s[4:5]
	global_load_dword v206, v[4:5], off
	v_add_co_u32_e64 v4, s[4:5], s61, v6
	s_nop 1
	v_addc_co_u32_e64 v5, s[4:5], 0, v7, s[4:5]
	global_load_dword v207, v[4:5], off
	v_lshl_add_u64 v[6:7], v[6:7], 0, s[6:7]
	global_load_dword v208, v[6:7], off
	v_add_co_u32_e64 v4, s[4:5], s44, v6
	s_nop 1
	v_addc_co_u32_e64 v5, s[4:5], 0, v7, s[4:5]
	global_load_dword v209, v[4:5], off
	v_add_co_u32_e64 v4, s[4:5], s48, v6
	s_nop 1
	v_addc_co_u32_e64 v5, s[4:5], 0, v7, s[4:5]
	global_load_dword v210, v[4:5], off
	v_add_co_u32_e64 v4, s[4:5], s49, v6
; __global__ void __launch_bounds__(NTHR, 2) mk_fwd(Args args) {
;     ...
;             for (int k0 = wave * 128; k0 < wave * 128 + 128; k0 += 16) {
;                 float wv[16];
; #pragma unroll
;                 for (int i = 0; i < 16; ++i) wv[i] = W[(size_t)(k0 + i) * (NMOD * DM)];
	s_nop 1
	v_addc_co_u32_e64 v5, s[4:5], 0, v7, s[4:5]
	global_load_dword v211, v[4:5], off
	v_add_co_u32_e64 v4, s[4:5], s50, v6
	s_nop 1
	v_addc_co_u32_e64 v5, s[4:5], 0, v7, s[4:5]
	global_load_dword v212, v[4:5], off
	v_add_co_u32_e64 v4, s[4:5], s51, v6
	s_nop 1
	v_addc_co_u32_e64 v5, s[4:5], 0, v7, s[4:5]
	global_load_dword v213, v[4:5], off
	v_add_co_u32_e64 v4, s[4:5], s52, v6
	s_nop 1
	v_addc_co_u32_e64 v5, s[4:5], 0, v7, s[4:5]
	global_load_dword v214, v[4:5], off
	v_add_co_u32_e64 v4, s[4:5], s53, v6
	s_nop 1
	v_addc_co_u32_e64 v5, s[4:5], 0, v7, s[4:5]
	global_load_dword v215, v[4:5], off
	v_add_co_u32_e64 v4, s[4:5], s54, v6
	s_nop 1
	v_addc_co_u32_e64 v5, s[4:5], 0, v7, s[4:5]
	global_load_dword v216, v[4:5], off
	v_add_co_u32_e64 v4, s[4:5], s55, v6
	s_nop 1
	v_addc_co_u32_e64 v5, s[4:5], 0, v7, s[4:5]
	global_load_dword v217, v[4:5], off
	v_add_co_u32_e64 v4, s[4:5], s56, v6
	s_nop 1
	v_addc_co_u32_e64 v5, s[4:5], 0, v7, s[4:5]
	global_load_dword v218, v[4:5], off
	v_add_co_u32_e64 v4, s[4:5], s57, v6
	s_nop 1
	v_addc_co_u32_e64 v5, s[4:5], 0, v7, s[4:5]
	global_load_dword v219, v[4:5], off
	v_add_co_u32_e64 v4, s[4:5], s58, v6
	s_nop 1
	v_addc_co_u32_e64 v5, s[4:5], 0, v7, s[4:5]
	global_load_dword v220, v[4:5], off
	v_add_co_u32_e64 v4, s[4:5], s59, v6
	s_nop 1
	v_addc_co_u32_e64 v5, s[4:5], 0, v7, s[4:5]
	global_load_dword v221, v[4:5], off
	v_add_co_u32_e64 v4, s[4:5], s60, v6
	s_nop 1
	v_addc_co_u32_e64 v5, s[4:5], 0, v7, s[4:5]
	global_load_dword v222, v[4:5], off
	v_add_co_u32_e64 v4, s[4:5], s61, v6
	s_nop 1
	v_addc_co_u32_e64 v5, s[4:5], 0, v7, s[4:5]
	global_load_dword v223, v[4:5], off
	v_lshl_add_u64 v[6:7], v[6:7], 0, s[6:7]
	global_load_dword v224, v[6:7], off
	v_add_co_u32_e64 v4, s[4:5], s44, v6
	s_nop 1
	v_addc_co_u32_e64 v5, s[4:5], 0, v7, s[4:5]
	global_load_dword v225, v[4:5], off
	v_add_co_u32_e64 v4, s[4:5], s48, v6
	s_nop 1
	v_addc_co_u32_e64 v5, s[4:5], 0, v7, s[4:5]
	global_load_dword v226, v[4:5], off
	v_add_co_u32_e64 v4, s[4:5], s49, v6
	s_nop 1
	v_addc_co_u32_e64 v5, s[4:5], 0, v7, s[4:5]
	global_load_dword v227, v[4:5], off
	v_add_co_u32_e64 v4, s[4:5], s50, v6
	s_nop 1
	v_addc_co_u32_e64 v5, s[4:5], 0, v7, s[4:5]
	global_load_dword v228, v[4:5], off
	v_add_co_u32_e64 v4, s[4:5], s51, v6
	s_nop 1
	v_addc_co_u32_e64 v5, s[4:5], 0, v7, s[4:5]
	global_load_dword v229, v[4:5], off
	v_add_co_u32_e64 v4, s[4:5], s52, v6
	s_nop 1
	v_addc_co_u32_e64 v5, s[4:5], 0, v7, s[4:5]
	global_load_dword v230, v[4:5], off
	v_add_co_u32_e64 v4, s[4:5], s53, v6
	s_nop 1
	v_addc_co_u32_e64 v5, s[4:5], 0, v7, s[4:5]
	global_load_dword v231, v[4:5], off
	v_add_co_u32_e64 v4, s[4:5], s54, v6
	s_nop 1
	v_addc_co_u32_e64 v5, s[4:5], 0, v7, s[4:5]
	global_load_dword v232, v[4:5], off
	v_add_co_u32_e64 v4, s[4:5], s55, v6
	s_nop 1
	v_addc_co_u32_e64 v5, s[4:5], 0, v7, s[4:5]
	global_load_dword v233, v[4:5], off
	v_add_co_u32_e64 v4, s[4:5], s56, v6
	s_nop 1
	v_addc_co_u32_e64 v5, s[4:5], 0, v7, s[4:5]
	global_load_dword v234, v[4:5], off
	v_add_co_u32_e64 v4, s[4:5], s57, v6
	s_nop 1
	v_addc_co_u32_e64 v5, s[4:5], 0, v7, s[4:5]
	global_load_dword v235, v[4:5], off
	v_add_co_u32_e64 v4, s[4:5], s58, v6
	s_nop 1
	v_addc_co_u32_e64 v5, s[4:5], 0, v7, s[4:5]
	global_load_dword v236, v[4:5], off
	v_add_co_u32_e64 v4, s[4:5], s59, v6
	s_nop 1
	v_addc_co_u32_e64 v5, s[4:5], 0, v7, s[4:5]
	global_load_dword v237, v[4:5], off
	v_add_co_u32_e64 v4, s[4:5], s60, v6
	s_nop 1
	v_addc_co_u32_e64 v5, s[4:5], 0, v7, s[4:5]
	global_load_dword v238, v[4:5], off
	v_add_co_u32_e64 v4, s[4:5], s61, v6
	s_nop 1
	v_addc_co_u32_e64 v5, s[4:5], 0, v7, s[4:5]
	global_load_dword v239, v[4:5], off
	v_lshl_add_u64 v[6:7], v[6:7], 0, s[6:7]
	global_load_dword v240, v[6:7], off
	v_add_co_u32_e64 v4, s[4:5], s44, v6
	s_nop 1
	v_addc_co_u32_e64 v5, s[4:5], 0, v7, s[4:5]
	global_load_dword v241, v[4:5], off
	v_add_co_u32_e64 v4, s[4:5], s48, v6
	s_nop 1
	v_addc_co_u32_e64 v5, s[4:5], 0, v7, s[4:5]
	global_load_dword v242, v[4:5], off
	v_add_co_u32_e64 v4, s[4:5], s49, v6
	s_nop 1
	v_addc_co_u32_e64 v5, s[4:5], 0, v7, s[4:5]
	global_load_dword v243, v[4:5], off
	v_add_co_u32_e64 v4, s[4:5], s50, v6
	s_nop 1
	v_addc_co_u32_e64 v5, s[4:5], 0, v7, s[4:5]
	global_load_dword v244, v[4:5], off
	v_add_co_u32_e64 v4, s[4:5], s51, v6
	s_nop 1
	v_addc_co_u32_e64 v5, s[4:5], 0, v7, s[4:5]
	global_load_dword v245, v[4:5], off
	v_add_co_u32_e64 v4, s[4:5], s52, v6
	s_nop 1
	v_addc_co_u32_e64 v5, s[4:5], 0, v7, s[4:5]
	global_load_dword v246, v[4:5], off
	v_add_co_u32_e64 v4, s[4:5], s53, v6
	s_nop 1
	v_addc_co_u32_e64 v5, s[4:5], 0, v7, s[4:5]
	global_load_dword v247, v[4:5], off
	v_add_co_u32_e64 v4, s[4:5], s54, v6
	s_nop 1
	v_addc_co_u32_e64 v5, s[4:5], 0, v7, s[4:5]
	global_load_dword v248, v[4:5], off
	v_add_co_u32_e64 v4, s[4:5], s55, v6
	s_nop 1
	v_addc_co_u32_e64 v5, s[4:5], 0, v7, s[4:5]
	global_load_dword v249, v[4:5], off
	v_add_co_u32_e64 v4, s[4:5], s56, v6
	s_nop 1
	v_addc_co_u32_e64 v5, s[4:5], 0, v7, s[4:5]
	global_load_dword v250, v[4:5], off
	v_add_co_u32_e64 v4, s[4:5], s57, v6
	s_nop 1
	v_addc_co_u32_e64 v5, s[4:5], 0, v7, s[4:5]
	global_load_dword v251, v[4:5], off
	v_add_co_u32_e64 v4, s[4:5], s58, v6
	s_nop 1
	v_addc_co_u32_e64 v5, s[4:5], 0, v7, s[4:5]
	global_load_dword v252, v[4:5], off
	v_add_co_u32_e64 v4, s[4:5], s59, v6
	s_nop 1
	v_addc_co_u32_e64 v5, s[4:5], 0, v7, s[4:5]
	global_load_dword v253, v[4:5], off
	v_add_co_u32_e64 v4, s[4:5], s60, v6
	s_nop 1
	v_addc_co_u32_e64 v5, s[4:5], 0, v7, s[4:5]
	global_load_dword v254, v[4:5], off
	v_add_co_u32_e64 v4, s[4:5], s61, v6
	s_nop 1
	v_addc_co_u32_e64 v5, s[4:5], 0, v7, s[4:5]
	global_load_dword v255, v[4:5], off
; __global__ void __launch_bounds__(NTHR, 2) mk_fwd(Args args) {
;     ...
;             for (int k0 = wave * 128; k0 < wave * 128 + 128; k0 += 16) {
;                 float wv[16];
; #pragma unroll
;                 for (int i = 0; i < 16; ++i) wv[i] = W[(size_t)(k0 + i) * (NMOD * DM)];
; #pragma unroll
;                 for (int i = 0; i < 16; ++i)
; #pragma unroll
;                     for (int r = 0; r < 17; ++r) acc[r] += sl[r * DM + k0 + i] * wv[i];
.LBB0_17:
	s_cmp_eq_u32 s98, 0
	s_cbranch_scc1 .Lgemv_c0
	s_cmp_eq_u32 s98, 1
	s_cbranch_scc1 .Lgemv_c1
	s_cmp_eq_u32 s98, 2
	s_cbranch_scc1 .Lgemv_c2
	s_cmp_eq_u32 s98, 3
	s_cbranch_scc1 .Lgemv_c3
	s_cmp_eq_u32 s98, 4
	s_cbranch_scc1 .Lgemv_c4
	s_cmp_eq_u32 s98, 5
	s_cbranch_scc1 .Lgemv_c5
	s_cmp_eq_u32 s98, 6
	s_cbranch_scc1 .Lgemv_c6
	s_branch .Lgemv_c7
.Lgemv_c0:
	s_waitcnt vmcnt(63)
	v_mov_b32_e32 v110, v128
	v_mov_b32_e32 v112, v129
	v_mov_b32_e32 v114, v130
	v_mov_b32_e32 v106, v131
	v_mov_b32_e32 v108, v132
	v_mov_b32_e32 v88, v133
	v_mov_b32_e32 v89, v134
	v_mov_b32_e32 v90, v135
	v_mov_b32_e32 v91, v136
	v_mov_b32_e32 v84, v137
	v_mov_b32_e32 v85, v138
	v_mov_b32_e32 v86, v139
	v_mov_b32_e32 v87, v140
	v_mov_b32_e32 v82, v141
	v_mov_b32_e32 v83, v142
	v_mov_b32_e32 v76, v143
	s_branch .Lgemv_go
.Lgemv_c1:
	s_waitcnt vmcnt(63)
	v_mov_b32_e32 v110, v144
	v_mov_b32_e32 v112, v145
	v_mov_b32_e32 v114, v146
	v_mov_b32_e32 v106, v147
	v_mov_b32_e32 v108, v148
	v_mov_b32_e32 v88, v149
	v_mov_b32_e32 v89, v150
	v_mov_b32_e32 v90, v151
	v_mov_b32_e32 v91, v152
	v_mov_b32_e32 v84, v153
	v_mov_b32_e32 v85, v154
	v_mov_b32_e32 v86, v155
	v_mov_b32_e32 v87, v156
	v_mov_b32_e32 v82, v157
	v_mov_b32_e32 v83, v158
	v_mov_b32_e32 v76, v159
	s_branch .Lgemv_go
.Lgemv_c2:
	s_waitcnt vmcnt(63)
	v_mov_b32_e32 v110, v160
	v_mov_b32_e32 v112, v161
	v_mov_b32_e32 v114, v162
	v_mov_b32_e32 v106, v163
	v_mov_b32_e32 v108, v164
	v_mov_b32_e32 v88, v165
	v_mov_b32_e32 v89, v166
	v_mov_b32_e32 v90, v167
	v_mov_b32_e32 v91, v168
	v_mov_b32_e32 v84, v169
	v_mov_b32_e32 v85, v170
	v_mov_b32_e32 v86, v171
	v_mov_b32_e32 v87, v172
	v_mov_b32_e32 v82, v173
	v_mov_b32_e32 v83, v174
	v_mov_b32_e32 v76, v175
	s_branch .Lgemv_go
.Lgemv_c3:
	s_waitcnt vmcnt(63)
	v_mov_b32_e32 v110, v176
	v_mov_b32_e32 v112, v177
	v_mov_b32_e32 v114, v178
	v_mov_b32_e32 v106, v179
	v_mov_b32_e32 v108, v180
	v_mov_b32_e32 v88, v181
	v_mov_b32_e32 v89, v182
	v_mov_b32_e32 v90, v183
	v_mov_b32_e32 v91, v184
	v_mov_b32_e32 v84, v185
	v_mov_b32_e32 v85, v186
	v_mov_b32_e32 v86, v187
	v_mov_b32_e32 v87, v188
	v_mov_b32_e32 v82, v189
	v_mov_b32_e32 v83, v190
	v_mov_b32_e32 v76, v191
	s_branch .Lgemv_go
.Lgemv_c4:
	s_waitcnt vmcnt(48)
	v_mov_b32_e32 v110, v192
	v_mov_b32_e32 v112, v193
	v_mov_b32_e32 v114, v194
	v_mov_b32_e32 v106, v195
	v_mov_b32_e32 v108, v196
	v_mov_b32_e32 v88, v197
	v_mov_b32_e32 v89, v198
	v_mov_b32_e32 v90, v199
	v_mov_b32_e32 v91, v200
	v_mov_b32_e32 v84, v201
	v_mov_b32_e32 v85, v202
	v_mov_b32_e32 v86, v203
	v_mov_b32_e32 v87, v204
	v_mov_b32_e32 v82, v205
	v_mov_b32_e32 v83, v206
	v_mov_b32_e32 v76, v207
	s_branch .Lgemv_go
.Lgemv_c5:
	s_waitcnt vmcnt(32)
	v_mov_b32_e32 v110, v208
	v_mov_b32_e32 v112, v209
	v_mov_b32_e32 v114, v210
	v_mov_b32_e32 v106, v211
	v_mov_b32_e32 v108, v212
	v_mov_b32_e32 v88, v213
	v_mov_b32_e32 v89, v214
	v_mov_b32_e32 v90, v215
	v_mov_b32_e32 v91, v216
	v_mov_b32_e32 v84, v217
	v_mov_b32_e32 v85, v218
	v_mov_b32_e32 v86, v219
	v_mov_b32_e32 v87, v220
	v_mov_b32_e32 v82, v221
	v_mov_b32_e32 v83, v222
	v_mov_b32_e32 v76, v223
	s_branch .Lgemv_go
.Lgemv_c6:
	s_waitcnt vmcnt(16)
	v_mov_b32_e32 v110, v224
	v_mov_b32_e32 v112, v225
	v_mov_b32_e32 v114, v226
	v_mov_b32_e32 v106, v227
	v_mov_b32_e32 v108, v228
	v_mov_b32_e32 v88, v229
	v_mov_b32_e32 v89, v230
	v_mov_b32_e32 v90, v231
	v_mov_b32_e32 v91, v232
	v_mov_b32_e32 v84, v233
	v_mov_b32_e32 v85, v234
	v_mov_b32_e32 v86, v235
	v_mov_b32_e32 v87, v236
	v_mov_b32_e32 v82, v237
	v_mov_b32_e32 v83, v238
	v_mov_b32_e32 v76, v239
	s_branch .Lgemv_go
.Lgemv_c7:
	s_waitcnt vmcnt(0)
	v_mov_b32_e32 v110, v240
	v_mov_b32_e32 v112, v241
	v_mov_b32_e32 v114, v242
	v_mov_b32_e32 v106, v243
	v_mov_b32_e32 v108, v244
	v_mov_b32_e32 v88, v245
	v_mov_b32_e32 v89, v246
	v_mov_b32_e32 v90, v247
	v_mov_b32_e32 v91, v248
	v_mov_b32_e32 v84, v249
	v_mov_b32_e32 v85, v250
	v_mov_b32_e32 v86, v251
	v_mov_b32_e32 v87, v252
	v_mov_b32_e32 v82, v253
	v_mov_b32_e32 v83, v254
	v_mov_b32_e32 v76, v255
.Lgemv_go:
	s_add_i32 s98, s98, 1
	v_add_co_u32_e64 v4, s[4:5], s44, v80
	s_nop 0
	v_addc_co_u32_e64 v5, s[4:5], 0, v81, s[4:5]
	v_add_co_u32_e64 v4, s[4:5], s48, v80
	v_mov_b32_e32 v111, s27
	s_nop 0
	v_addc_co_u32_e64 v5, s[4:5], 0, v81, s[4:5]
	v_add_co_u32_e64 v4, s[4:5], s49, v80
	s_add_i32 s68, s27, 0x11800
	s_nop 0
	v_addc_co_u32_e64 v5, s[4:5], 0, v81, s[4:5]
	v_add_co_u32_e64 v4, s[4:5], s50, v80
	s_add_i32 s70, s27, 0x10810
	s_nop 0
	v_addc_co_u32_e64 v5, s[4:5], 0, v81, s[4:5]
	v_add_co_u32_e64 v4, s[4:5], s51, v80
	s_add_i32 s69, s27, 0x10800
	s_nop 0
	v_addc_co_u32_e64 v5, s[4:5], 0, v81, s[4:5]
	v_add_co_u32_e64 v4, s[4:5], s52, v80
	s_add_i32 s66, s27, 0x13800
	s_nop 0
	v_addc_co_u32_e64 v5, s[4:5], 0, v81, s[4:5]
	v_add_co_u32_e64 v4, s[4:5], s53, v80
	s_add_i32 s67, s27, 0x12800
	s_nop 0
	v_addc_co_u32_e64 v5, s[4:5], 0, v81, s[4:5]
	v_add_co_u32_e64 v4, s[4:5], s54, v80
	s_add_i32 s29, s27, 0x15800
	s_nop 0
	v_addc_co_u32_e64 v5, s[4:5], 0, v81, s[4:5]
	v_add_co_u32_e64 v4, s[4:5], s55, v80
	s_add_i32 s65, s27, 0x14800
	s_nop 0
	v_addc_co_u32_e64 v5, s[4:5], 0, v81, s[4:5]
	v_add_co_u32_e64 v4, s[4:5], s56, v80
	s_add_i32 s28, s27, 0x16800
	s_nop 0
	v_addc_co_u32_e64 v5, s[4:5], 0, v81, s[4:5]
	v_add_co_u32_e64 v4, s[4:5], s57, v80
	s_add_i32 s77, s27, 0x1882c
	s_nop 0
	v_addc_co_u32_e64 v5, s[4:5], 0, v81, s[4:5]
	v_add_co_u32_e64 v4, s[4:5], s58, v80
	s_add_i32 s76, s27, 0x10820
	s_nop 0
	v_addc_co_u32_e64 v5, s[4:5], 0, v81, s[4:5]
	v_add_co_u32_e64 v4, s[4:5], s59, v80
	s_add_i32 s75, s27, 0x11820
	s_nop 0
	v_addc_co_u32_e64 v5, s[4:5], 0, v81, s[4:5]
	v_add_co_u32_e64 v4, s[4:5], s60, v80
	s_add_i32 s74, s27, 0x10830
	s_nop 0
	v_addc_co_u32_e64 v5, s[4:5], 0, v81, s[4:5]
	v_add_co_u32_e64 v4, s[4:5], s61, v80
	s_add_i32 s73, s27, 0x11830
	s_nop 0
	v_addc_co_u32_e64 v5, s[4:5], 0, v81, s[4:5]
	s_add_i32 s4, s27, 0x18800
	v_mov_b32_e32 v4, s4
	ds_read_b96 v[4:6], v4
	s_add_i32 s5, s27, 0x17800
	s_add_i32 s4, s27, 0x1880c
	s_add_i32 s72, s27, 0x12820
	s_add_i32 s71, s27, 0x13820
	s_waitcnt lgkmcnt(0)
; __global__ void __launch_bounds__(NTHR, 2) mk_fwd(Args args) {
;     ...
; #pragma unroll
;                 for (int i = 0; i < 16; ++i)
; #pragma unroll
;                     for (int r = 0; r < 17; ++r) acc[r] += sl[r * DM + k0 + i] * wv[i];
	v_fmac_f32_e32 v109, v4, v110
	v_fmac_f32_e32 v109, v5, v112
	v_fmac_f32_e32 v109, v6, v114
	ds_read_b128 v[4:7], v111 offset:34816
	ds_read_b128 v[66:69], v111 offset:34832
	ds_read_b128 v[62:65], v111 offset:34848
	ds_read_b128 v[50:53], v111 offset:34864
	ds_read_b128 v[70:73], v111 offset:38928
	ds_read_b128 v[12:15], v111 offset:38912
	s_waitcnt lgkmcnt(5)
	v_mov_b32_e32 v8, v4
	v_mov_b32_e32 v4, v6
	s_add_i32 s26, s26, 16
	v_lshl_add_u64 v[80:81], v[80:81], 0, s[6:7]
	s_waitcnt lgkmcnt(0)
	v_mov_b32_e32 v9, v12
	v_pk_fma_f32 v[2:3], v[8:9], v[110:111], v[2:3] op_sel_hi:[1,0,1]
	v_mov_b32_e32 v12, v5
	v_pk_fma_f32 v[2:3], v[12:13], v[112:113], v[2:3] op_sel_hi:[1,0,1]
	v_mov_b32_e32 v5, v14
	v_pk_fma_f32 v[2:3], v[4:5], v[114:115], v[2:3] op_sel_hi:[1,0,1]
	v_mov_b32_e32 v14, v7
	v_pk_fma_f32 v[2:3], v[14:15], v[106:107], v[2:3] op_sel_hi:[1,0,1]
	v_mov_b32_e32 v4, v66
	v_mov_b32_e32 v5, v70
	v_pk_fma_f32 v[116:117], v[4:5], v[108:109], v[2:3] op_sel_hi:[1,0,1]
	ds_read_b128 v[54:57], v111 offset:43024
	ds_read_b128 v[58:61], v111 offset:47120
	ds_read_b128 v[2:5], v111 offset:43008
	ds_read_b128 v[6:9], v111 offset:47104
	v_mov_b32_e32 v70, v67
	s_waitcnt lgkmcnt(1)
	v_mov_b32_e32 v12, v2
	s_waitcnt lgkmcnt(0)
	v_mov_b32_e32 v13, v6
	v_pk_fma_f32 v[10:11], v[12:13], v[110:111], v[10:11] op_sel_hi:[1,0,1]
	v_mov_b32_e32 v6, v3
	v_pk_fma_f32 v[2:3], v[6:7], v[112:113], v[10:11] op_sel_hi:[1,0,1]
	v_mov_b32_e32 v6, v4
	v_mov_b32_e32 v7, v8
	v_pk_fma_f32 v[2:3], v[6:7], v[114:115], v[2:3] op_sel_hi:[1,0,1]
	v_mov_b32_e32 v8, v5
	v_pk_fma_f32 v[2:3], v[8:9], v[106:107], v[2:3] op_sel_hi:[1,0,1]
	v_mov_b32_e32 v4, v54
	v_mov_b32_e32 v5, v58
	v_pk_fma_f32 v[104:105], v[4:5], v[108:109], v[2:3] op_sel_hi:[1,0,1]
	ds_read_b128 v[42:45], v111 offset:51216
	ds_read_b128 v[46:49], v111 offset:55312
	ds_read_b128 v[2:5], v111 offset:51200
	ds_read_b128 v[6:9], v111 offset:55296
	v_mov_b32_e32 v58, v55
	s_waitcnt lgkmcnt(1)
	v_mov_b32_e32 v10, v2
	s_waitcnt lgkmcnt(0)
	v_mov_b32_e32 v11, v6
	v_pk_fma_f32 v[10:11], v[10:11], v[110:111], v[18:19] op_sel_hi:[1,0,1]
	v_mov_b32_e32 v6, v3
	v_pk_fma_f32 v[2:3], v[6:7], v[112:113], v[10:11] op_sel_hi:[1,0,1]
	v_mov_b32_e32 v6, v4
	v_mov_b32_e32 v7, v8
	v_pk_fma_f32 v[2:3], v[6:7], v[114:115], v[2:3] op_sel_hi:[1,0,1]
	v_mov_b32_e32 v8, v5
	v_pk_fma_f32 v[2:3], v[8:9], v[106:107], v[2:3] op_sel_hi:[1,0,1]
	v_mov_b32_e32 v4, v42
	v_mov_b32_e32 v5, v46
	v_pk_fma_f32 v[102:103], v[4:5], v[108:109], v[2:3] op_sel_hi:[1,0,1]
	ds_read_b128 v[26:29], v111 offset:59408
	ds_read_b128 v[30:33], v111 offset:63504
	ds_read_b128 v[2:5], v111 offset:59392
	ds_read_b128 v[6:9], v111 offset:63488
	v_mov_b32_e32 v42, v91
	v_mov_b32_e32 v54, v85
	v_mov_b32_e32 v46, v43
	s_waitcnt lgkmcnt(1)
	v_mov_b32_e32 v10, v2
	s_waitcnt lgkmcnt(0)
	v_mov_b32_e32 v11, v6
	v_pk_fma_f32 v[10:11], v[10:11], v[110:111], v[34:35] op_sel_hi:[1,0,1]
	v_mov_b32_e32 v6, v3
	v_pk_fma_f32 v[2:3], v[6:7], v[112:113], v[10:11] op_sel_hi:[1,0,1]
	v_mov_b32_e32 v6, v4
	v_mov_b32_e32 v7, v8
	v_pk_fma_f32 v[2:3], v[6:7], v[114:115], v[2:3] op_sel_hi:[1,0,1]
	v_mov_b32_e32 v8, v5
	v_pk_fma_f32 v[2:3], v[8:9], v[106:107], v[2:3] op_sel_hi:[1,0,1]
	v_mov_b32_e32 v4, v26
	v_mov_b32_e32 v5, v30
	v_pk_fma_f32 v[100:101], v[4:5], v[108:109], v[2:3] op_sel_hi:[1,0,1]
	v_mov_b32_e32 v2, s70
	s_add_i32 s70, s27, 0x11810
	v_mov_b32_e32 v6, s68
	ds_read_b128 v[34:37], v2
	ds_read_b128 v[6:9], v6
	v_mov_b32_e32 v2, s70
	ds_read_b128 v[38:41], v2
	v_mov_b32_e32 v2, s69
	ds_read_b128 v[2:5], v2
	s_waitcnt lgkmcnt(2)
	v_mov_b32_e32 v11, v6
	s_add_i32 s68, s27, 0x12810
	v_mov_b32_e32 v26, v89
	v_mov_b32_e32 v30, v27
	s_waitcnt lgkmcnt(0)
	v_mov_b32_e32 v10, v2
	v_pk_fma_f32 v[10:11], v[10:11], v[110:111], v[92:93] op_sel_hi:[1,0,1]
	v_mov_b32_e32 v6, v3
	v_pk_fma_f32 v[2:3], v[6:7], v[112:113], v[10:11] op_sel_hi:[1,0,1]
	v_mov_b32_e32 v6, v4
	v_mov_b32_e32 v7, v8
	v_pk_fma_f32 v[2:3], v[6:7], v[114:115], v[2:3] op_sel_hi:[1,0,1]
	v_mov_b32_e32 v8, v5
	v_pk_fma_f32 v[2:3], v[8:9], v[106:107], v[2:3] op_sel_hi:[1,0,1]
	v_mov_b32_e32 v4, v34
	v_mov_b32_e32 v5, v38
	v_pk_fma_f32 v[92:93], v[4:5], v[108:109], v[2:3] op_sel_hi:[1,0,1]
	v_mov_b32_e32 v2, s68
	s_add_i32 s68, s27, 0x13810
	v_mov_b32_e32 v6, s66
	ds_read_b128 v[18:21], v2
	ds_read_b128 v[6:9], v6
	v_mov_b32_e32 v2, s68
	ds_read_b128 v[22:25], v2
	v_mov_b32_e32 v2, s67
	ds_read_b128 v[2:5], v2
	s_waitcnt lgkmcnt(2)
	v_mov_b32_e32 v11, v6
	s_add_i32 s66, s27, 0x14810
	v_mov_b32_e32 v38, v35
	v_mov_b32_e32 v34, v44
	s_waitcnt lgkmcnt(0)
	v_mov_b32_e32 v10, v2
	v_pk_fma_f32 v[10:11], v[10:11], v[110:111], v[96:97] op_sel_hi:[1,0,1]
	v_mov_b32_e32 v6, v3
	v_pk_fma_f32 v[2:3], v[6:7], v[112:113], v[10:11] op_sel_hi:[1,0,1]
	v_mov_b32_e32 v6, v4
	v_mov_b32_e32 v7, v8
	v_pk_fma_f32 v[2:3], v[6:7], v[114:115], v[2:3] op_sel_hi:[1,0,1]
	v_mov_b32_e32 v8, v5
	v_pk_fma_f32 v[2:3], v[8:9], v[106:107], v[2:3] op_sel_hi:[1,0,1]
	v_mov_b32_e32 v4, v18
	v_mov_b32_e32 v5, v22
	v_pk_fma_f32 v[96:97], v[4:5], v[108:109], v[2:3] op_sel_hi:[1,0,1]
	v_mov_b32_e32 v2, s66
	s_add_i32 s66, s27, 0x15810
	v_mov_b32_e32 v6, s29
	ds_read_b128 v[10:13], v2
	ds_read_b128 v[6:9], v6
	v_mov_b32_e32 v2, s66
	ds_read_b128 v[14:17], v2
	v_mov_b32_e32 v2, s65
	ds_read_b128 v[2:5], v2
	s_waitcnt lgkmcnt(2)
	v_mov_b32_e32 v119, v6
	s_add_i32 s29, s27, 0x16810
	v_mov_b32_e32 v22, v19
	v_mov_b32_e32 v18, v56
	s_waitcnt lgkmcnt(0)
; __global__ void __launch_bounds__(NTHR, 2) mk_fwd(Args args) {
;     ...
; #pragma unroll
;                 for (int i = 0; i < 16; ++i)
; #pragma unroll
;                     for (int r = 0; r < 17; ++r) acc[r] += sl[r * DM + k0 + i] * wv[i];
	v_mov_b32_e32 v118, v2
	v_pk_fma_f32 v[98:99], v[118:119], v[110:111], v[98:99] op_sel_hi:[1,0,1]
	v_mov_b32_e32 v6, v3
	v_pk_fma_f32 v[2:3], v[6:7], v[112:113], v[98:99] op_sel_hi:[1,0,1]
	v_mov_b32_e32 v6, v4
	v_mov_b32_e32 v4, v10
	v_mov_b32_e32 v10, s28
	v_mov_b32_e32 v7, v8
	ds_read_b128 v[118:121], v10
	v_mov_b32_e32 v10, s5
	v_pk_fma_f32 v[2:3], v[6:7], v[114:115], v[2:3] op_sel_hi:[1,0,1]
	v_mov_b32_e32 v8, v5
	ds_read_b128 v[122:125], v10
	v_pk_fma_f32 v[2:3], v[8:9], v[106:107], v[2:3] op_sel_hi:[1,0,1]
	v_mov_b32_e32 v5, v14
	v_pk_fma_f32 v[98:99], v[4:5], v[108:109], v[2:3] op_sel_hi:[1,0,1]
	v_mov_b32_e32 v2, s29
	s_add_i32 s29, s27, 0x17810
	v_mov_b32_e32 v6, s29
	ds_read_b128 v[2:5], v2
	ds_read_b128 v[6:9], v6
	s_waitcnt lgkmcnt(3)
	v_mov_b32_e32 v126, v118
	s_waitcnt lgkmcnt(2)
	v_mov_b32_e32 v127, v122
	v_pk_fma_f32 v[94:95], v[126:127], v[110:111], v[94:95] op_sel_hi:[1,0,1]
	v_mov_b32_e32 v122, v119
	v_pk_fma_f32 v[94:95], v[122:123], v[112:113], v[94:95] op_sel_hi:[1,0,1]
	v_mov_b32_e32 v112, v120
	v_mov_b32_e32 v113, v124
	v_pk_fma_f32 v[94:95], v[112:113], v[114:115], v[94:95] op_sel_hi:[1,0,1]
	v_mov_b32_e32 v124, v121
	v_pk_fma_f32 v[94:95], v[124:125], v[106:107], v[94:95] op_sel_hi:[1,0,1]
	s_waitcnt lgkmcnt(1)
	v_mov_b32_e32 v112, v2
	s_waitcnt lgkmcnt(0)
	v_mov_b32_e32 v113, v6
	v_mov_b32_e32 v2, s4
	v_pk_fma_f32 v[94:95], v[112:113], v[108:109], v[94:95] op_sel_hi:[1,0,1]
	ds_read2_b32 v[112:113], v2 offset1:1
	v_mov_b32_e32 v107, v108
	s_add_i32 s4, s27, 0x18814
	v_mov_b32_e32 v6, v3
	v_mov_b32_e32 v14, v11
	s_waitcnt lgkmcnt(0)
	v_pk_mul_f32 v[106:107], v[112:113], v[106:107]
	v_mov_b32_e32 v11, v72
	v_add_f32_e32 v2, v109, v106
	v_add_f32_e32 v10, v2, v107
	v_mov_b32_e32 v2, s4
	ds_read2_b32 v[2:3], v2 offset1:1
	s_add_i32 s4, s27, 0x1881c
	v_mov_b32_e32 v72, v69
	v_mov_b32_e32 v19, v60
	v_mov_b32_e32 v60, v57
	s_waitcnt lgkmcnt(0)
	v_pk_mul_f32 v[2:3], v[2:3], v[88:89]
	v_mov_b32_e32 v35, v48
	v_add_f32_e32 v2, v10, v2
	v_add_f32_e32 v10, v2, v3
	v_mov_b32_e32 v2, s4
	ds_read2_b32 v[2:3], v2 offset1:1
	s_add_i32 s4, s27, 0x18824
	v_mov_b32_e32 v48, v45
	v_pk_fma_f32 v[30:31], v[30:31], v[88:89], v[100:101] op_sel_hi:[1,0,1]
	v_pk_fma_f32 v[22:23], v[22:23], v[88:89], v[96:97] op_sel_hi:[1,0,1]
	s_waitcnt lgkmcnt(0)
	v_pk_mul_f32 v[2:3], v[2:3], v[90:91]
	s_add_i32 s70, s27, 0x12830
	v_add_f32_e32 v2, v10, v2
	v_add_f32_e32 v10, v2, v3
	v_mov_b32_e32 v2, s4
	ds_read2_b32 v[2:3], v2 offset1:1
	s_add_i32 s69, s27, 0x13830
	s_add_i32 s68, s27, 0x14820
	s_add_i32 s67, s27, 0x15820
	v_pk_fma_f32 v[14:15], v[14:15], v[88:89], v[98:99] op_sel_hi:[1,0,1]
	s_waitcnt lgkmcnt(0)
	v_pk_mul_f32 v[2:3], v[2:3], v[84:85]
	s_add_i32 s66, s27, 0x14830
	v_add_f32_e32 v2, v10, v2
	v_add_f32_e32 v10, v2, v3
	v_mov_b32_e32 v2, s77
	ds_read2_b32 v[2:3], v2 offset1:1
	s_add_i32 s77, s27, 0x18834
	s_add_i32 s65, s27, 0x15830
	s_add_i32 s29, s27, 0x16820
	s_add_i32 s28, s27, 0x17820
	s_waitcnt lgkmcnt(0)
	v_pk_mul_f32 v[2:3], v[2:3], v[86:87]
	v_pk_fma_f32 v[6:7], v[6:7], v[88:89], v[94:95] op_sel_hi:[1,0,1]
	v_add_f32_e32 v2, v10, v2
	v_add_f32_e32 v10, v2, v3
	v_mov_b32_e32 v2, s77
	ds_read2_b32 v[2:3], v2 offset1:1
	s_add_i32 s5, s27, 0x16830
	s_add_i32 s4, s27, 0x17830
	s_waitcnt lgkmcnt(0)
	v_pk_mul_f32 v[2:3], v[2:3], v[82:83]
	s_nop 0
	v_add_f32_e32 v2, v10, v2
	v_mov_b32_e32 v10, v68
	ds_read_b128 v[66:69], v111 offset:38944
	v_add_f32_e32 v109, v2, v3
	v_pk_fma_f32 v[2:3], v[70:71], v[88:89], v[116:117] op_sel_hi:[1,0,1]
	s_nop 0
	v_pk_fma_f32 v[2:3], v[10:11], v[26:27], v[2:3] op_sel_hi:[1,0,1]
	v_mov_b32_e32 v10, v62
	v_pk_fma_f32 v[2:3], v[72:73], v[90:91], v[2:3] op_sel_hi:[1,0,1]
	s_waitcnt lgkmcnt(0)
	v_mov_b32_e32 v11, v66
	v_pk_fma_f32 v[2:3], v[10:11], v[42:43], v[2:3] op_sel_hi:[1,0,1]
	v_mov_b32_e32 v66, v63
	v_mov_b32_e32 v10, v64
	v_mov_b32_e32 v11, v68
	v_mov_b32_e32 v68, v65
	ds_read_b128 v[62:65], v111 offset:38960
	v_pk_fma_f32 v[2:3], v[66:67], v[84:85], v[2:3] op_sel_hi:[1,0,1]
	s_nop 0
	v_pk_fma_f32 v[2:3], v[10:11], v[54:55], v[2:3] op_sel_hi:[1,0,1]
	v_mov_b32_e32 v10, v50
	v_pk_fma_f32 v[2:3], v[68:69], v[86:87], v[2:3] op_sel_hi:[1,0,1]
	s_waitcnt lgkmcnt(0)
	v_mov_b32_e32 v11, v62
	v_mov_b32_e32 v50, v87
	v_pk_fma_f32 v[2:3], v[10:11], v[50:51], v[2:3] op_sel_hi:[1,0,1]
	v_mov_b32_e32 v62, v51
	v_pk_fma_f32 v[2:3], v[62:63], v[82:83], v[2:3] op_sel_hi:[1,0,1]
	v_mov_b32_e32 v10, v52
	v_mov_b32_e32 v11, v64
	v_mov_b32_e32 v52, v83
	v_pk_fma_f32 v[2:3], v[10:11], v[52:53], v[2:3] op_sel_hi:[1,0,1]
	v_pk_fma_f32 v[10:11], v[58:59], v[88:89], v[104:105] op_sel_hi:[1,0,1]
	v_mov_b32_e32 v64, v53
	v_pk_fma_f32 v[10:11], v[18:19], v[26:27], v[10:11] op_sel_hi:[1,0,1]
	v_pk_fma_f32 v[2:3], v[64:65], v[76:77], v[2:3] op_sel_hi:[1,0,1]
	v_pk_fma_f32 v[10:11], v[60:61], v[90:91], v[10:11] op_sel_hi:[1,0,1]
	ds_read_b128 v[56:59], v111 offset:43040
	ds_read_b128 v[60:63], v111 offset:47136
	s_waitcnt lgkmcnt(1)
	v_mov_b32_e32 v18, v56
	s_waitcnt lgkmcnt(0)
	v_mov_b32_e32 v19, v60
	v_pk_fma_f32 v[10:11], v[18:19], v[42:43], v[10:11] op_sel_hi:[1,0,1]
	v_mov_b32_e32 v60, v57
	v_pk_fma_f32 v[10:11], v[60:61], v[84:85], v[10:11] op_sel_hi:[1,0,1]
	v_mov_b32_e32 v18, v58
	v_mov_b32_e32 v19, v62
	v_pk_fma_f32 v[10:11], v[18:19], v[54:55], v[10:11] op_sel_hi:[1,0,1]
	v_mov_b32_e32 v62, v59
	v_pk_fma_f32 v[10:11], v[62:63], v[86:87], v[10:11] op_sel_hi:[1,0,1]
	ds_read_b128 v[56:59], v111 offset:43056
	ds_read_b128 v[60:63], v111 offset:47152
	s_waitcnt lgkmcnt(1)
	v_mov_b32_e32 v18, v56
	s_waitcnt lgkmcnt(0)
; __global__ void __launch_bounds__(NTHR, 2) mk_fwd(Args args) {
;     ...
; #pragma unroll
;                 for (int i = 0; i < 16; ++i)
; #pragma unroll
;                     for (int r = 0; r < 17; ++r) acc[r] += sl[r * DM + k0 + i] * wv[i];
	v_mov_b32_e32 v19, v60
	v_pk_fma_f32 v[10:11], v[18:19], v[50:51], v[10:11] op_sel_hi:[1,0,1]
	v_mov_b32_e32 v60, v57
	v_pk_fma_f32 v[10:11], v[60:61], v[82:83], v[10:11] op_sel_hi:[1,0,1]
	v_mov_b32_e32 v18, v58
	v_mov_b32_e32 v19, v62
	v_pk_fma_f32 v[10:11], v[18:19], v[52:53], v[10:11] op_sel_hi:[1,0,1]
	v_mov_b32_e32 v62, v59
	v_pk_fma_f32 v[18:19], v[46:47], v[88:89], v[102:103] op_sel_hi:[1,0,1]
	ds_read_b128 v[44:47], v111 offset:51232
	ds_read_b128 v[56:59], v111 offset:55328
	v_pk_fma_f32 v[18:19], v[34:35], v[26:27], v[18:19] op_sel_hi:[1,0,1]
	v_pk_fma_f32 v[10:11], v[62:63], v[76:77], v[10:11] op_sel_hi:[1,0,1]
	v_pk_fma_f32 v[18:19], v[48:49], v[90:91], v[18:19] op_sel_hi:[1,0,1]
	s_waitcnt lgkmcnt(1)
	v_mov_b32_e32 v34, v44
	s_waitcnt lgkmcnt(0)
	v_mov_b32_e32 v35, v56
	v_pk_fma_f32 v[18:19], v[34:35], v[42:43], v[18:19] op_sel_hi:[1,0,1]
	v_mov_b32_e32 v56, v45
	v_pk_fma_f32 v[18:19], v[56:57], v[84:85], v[18:19] op_sel_hi:[1,0,1]
	v_mov_b32_e32 v34, v46
	v_mov_b32_e32 v35, v58
	v_pk_fma_f32 v[18:19], v[34:35], v[54:55], v[18:19] op_sel_hi:[1,0,1]
	v_mov_b32_e32 v58, v47
	v_pk_fma_f32 v[18:19], v[58:59], v[86:87], v[18:19] op_sel_hi:[1,0,1]
	ds_read_b128 v[44:47], v111 offset:51248
	ds_read_b128 v[56:59], v111 offset:55344
	s_waitcnt lgkmcnt(1)
	v_mov_b32_e32 v34, v44
	s_waitcnt lgkmcnt(0)
	v_mov_b32_e32 v35, v56
	v_pk_fma_f32 v[18:19], v[34:35], v[50:51], v[18:19] op_sel_hi:[1,0,1]
	v_mov_b32_e32 v56, v45
	v_pk_fma_f32 v[18:19], v[56:57], v[82:83], v[18:19] op_sel_hi:[1,0,1]
	v_mov_b32_e32 v34, v46
	v_mov_b32_e32 v35, v58
	v_pk_fma_f32 v[18:19], v[34:35], v[52:53], v[18:19] op_sel_hi:[1,0,1]
	v_mov_b32_e32 v34, v28
	v_mov_b32_e32 v35, v32
	v_pk_fma_f32 v[30:31], v[34:35], v[26:27], v[30:31] op_sel_hi:[1,0,1]
	v_mov_b32_e32 v32, v29
	v_pk_fma_f32 v[44:45], v[32:33], v[90:91], v[30:31] op_sel_hi:[1,0,1]
	ds_read_b128 v[28:31], v111 offset:59424
	ds_read_b128 v[32:35], v111 offset:63520
	v_mov_b32_e32 v58, v47
	v_pk_fma_f32 v[18:19], v[58:59], v[76:77], v[18:19] op_sel_hi:[1,0,1]
	s_waitcnt lgkmcnt(1)
	v_mov_b32_e32 v46, v28
	s_waitcnt lgkmcnt(0)
	v_mov_b32_e32 v47, v32
	v_pk_fma_f32 v[44:45], v[46:47], v[42:43], v[44:45] op_sel_hi:[1,0,1]
	v_mov_b32_e32 v32, v29
	v_pk_fma_f32 v[28:29], v[32:33], v[84:85], v[44:45] op_sel_hi:[1,0,1]
	v_mov_b32_e32 v32, v30
	v_mov_b32_e32 v33, v34
	v_pk_fma_f32 v[28:29], v[32:33], v[54:55], v[28:29] op_sel_hi:[1,0,1]
	v_mov_b32_e32 v34, v31
	v_pk_fma_f32 v[44:45], v[34:35], v[86:87], v[28:29] op_sel_hi:[1,0,1]
	ds_read_b128 v[28:31], v111 offset:59440
	ds_read_b128 v[32:35], v111 offset:63536
	s_waitcnt lgkmcnt(1)
	v_mov_b32_e32 v46, v28
	s_waitcnt lgkmcnt(0)
	v_mov_b32_e32 v47, v32
	v_pk_fma_f32 v[44:45], v[46:47], v[50:51], v[44:45] op_sel_hi:[1,0,1]
	v_mov_b32_e32 v32, v29
	v_pk_fma_f32 v[28:29], v[32:33], v[82:83], v[44:45] op_sel_hi:[1,0,1]
	v_mov_b32_e32 v32, v30
	v_mov_b32_e32 v33, v34
	v_pk_fma_f32 v[28:29], v[32:33], v[52:53], v[28:29] op_sel_hi:[1,0,1]
	v_mov_b32_e32 v34, v31
	v_pk_fma_f32 v[34:35], v[34:35], v[76:77], v[28:29] op_sel_hi:[1,0,1]
	v_pk_fma_f32 v[28:29], v[38:39], v[88:89], v[92:93] op_sel_hi:[1,0,1]
	v_mov_b32_e32 v30, v36
	v_mov_b32_e32 v31, v40
	v_pk_fma_f32 v[28:29], v[30:31], v[26:27], v[28:29] op_sel_hi:[1,0,1]
	v_mov_b32_e32 v27, s76
	ds_read_b128 v[30:33], v27
	v_mov_b32_e32 v27, s75
	v_mov_b32_e32 v40, v37
	ds_read_b128 v[36:39], v27
	v_pk_fma_f32 v[28:29], v[40:41], v[90:91], v[28:29] op_sel_hi:[1,0,1]
	s_waitcnt lgkmcnt(1)
	v_mov_b32_e32 v40, v30
	v_mov_b32_e32 v30, v32
	v_mov_b32_e32 v27, s74
	s_waitcnt lgkmcnt(0)
	v_mov_b32_e32 v41, v36
	v_pk_fma_f32 v[28:29], v[40:41], v[42:43], v[28:29] op_sel_hi:[1,0,1]
	v_mov_b32_e32 v36, v31
	v_pk_fma_f32 v[28:29], v[36:37], v[84:85], v[28:29] op_sel_hi:[1,0,1]
	v_mov_b32_e32 v31, v38
	v_pk_fma_f32 v[28:29], v[30:31], v[54:55], v[28:29] op_sel_hi:[1,0,1]
	v_mov_b32_e32 v38, v33
	v_pk_fma_f32 v[32:33], v[38:39], v[86:87], v[28:29] op_sel_hi:[1,0,1]
	ds_read_b128 v[28:31], v27
	v_mov_b32_e32 v27, s73
	ds_read_b128 v[36:39], v27
	s_waitcnt lgkmcnt(1)
	v_mov_b32_e32 v40, v28
	s_waitcnt lgkmcnt(0)
	v_mov_b32_e32 v41, v36
	v_pk_fma_f32 v[32:33], v[40:41], v[50:51], v[32:33] op_sel_hi:[1,0,1]
	v_mov_b32_e32 v36, v29
	v_pk_fma_f32 v[28:29], v[36:37], v[82:83], v[32:33] op_sel_hi:[1,0,1]
	v_mov_b32_e32 v32, v30
	v_mov_b32_e32 v33, v38
	v_pk_fma_f32 v[28:29], v[32:33], v[52:53], v[28:29] op_sel_hi:[1,0,1]
	v_mov_b32_e32 v38, v31
	v_pk_fma_f32 v[92:93], v[38:39], v[76:77], v[28:29] op_sel_hi:[1,0,1]
	v_mov_b32_e32 v28, v20
	v_mov_b32_e32 v29, v24
	v_pk_fma_f32 v[22:23], v[28:29], v[26:27], v[22:23] op_sel_hi:[1,0,1]
	v_mov_b32_e32 v24, v21
	v_mov_b32_e32 v20, s72
	v_mov_b32_e32 v27, s71
	v_pk_fma_f32 v[24:25], v[24:25], v[90:91], v[22:23] op_sel_hi:[1,0,1]
	ds_read_b128 v[20:23], v20
	ds_read_b128 v[28:31], v27
	v_mov_b32_e32 v27, s69
	s_waitcnt lgkmcnt(1)
; __global__ void __launch_bounds__(NTHR, 2) mk_fwd(Args args) {
;     ...
; #pragma unroll
;                 for (int i = 0; i < 16; ++i)
; #pragma unroll
;                     for (int r = 0; r < 17; ++r) acc[r] += sl[r * DM + k0 + i] * wv[i];
;             }
; #pragma unroll
;             for (int r = 0; r < 17; ++r) red[(wave * 17 + r) * 64 + lane] = acc[r];
;             __syncthreads();
;             for (int idx = tid; idx < 17 * 64; idx += NTHR) {
;                 const int r = idx >> 6, ln = idx & 63; float sm = 0.f;
; #pragma unroll
;                 for (int ww = 0; ww < 8; ++ww) sm += red[(ww * 17 + r) * 64 + ln];
;                 mod[((size_t)l * 17 + r) * (NMOD * DM) + nb * 64 + ln] = sm + b_mod[l * (NMOD * DM) + nb * 64 + ln];
	v_mov_b32_e32 v32, v20
	s_waitcnt lgkmcnt(0)
	v_mov_b32_e32 v33, v28
	v_pk_fma_f32 v[24:25], v[32:33], v[42:43], v[24:25] op_sel_hi:[1,0,1]
	v_mov_b32_e32 v28, v21
	v_pk_fma_f32 v[20:21], v[28:29], v[84:85], v[24:25] op_sel_hi:[1,0,1]
	v_mov_b32_e32 v24, v22
	v_mov_b32_e32 v25, v30
	v_pk_fma_f32 v[20:21], v[24:25], v[54:55], v[20:21] op_sel_hi:[1,0,1]
	v_mov_b32_e32 v30, v23
	v_pk_fma_f32 v[24:25], v[30:31], v[86:87], v[20:21] op_sel_hi:[1,0,1]
	v_mov_b32_e32 v20, s70
	ds_read_b128 v[20:23], v20
	ds_read_b128 v[28:31], v27
	s_waitcnt lgkmcnt(1)
	v_mov_b32_e32 v32, v20
	s_waitcnt lgkmcnt(0)
	v_mov_b32_e32 v33, v28
	v_pk_fma_f32 v[24:25], v[32:33], v[50:51], v[24:25] op_sel_hi:[1,0,1]
	v_mov_b32_e32 v28, v21
	v_pk_fma_f32 v[20:21], v[28:29], v[82:83], v[24:25] op_sel_hi:[1,0,1]
	v_mov_b32_e32 v24, v22
	v_mov_b32_e32 v25, v30
	v_pk_fma_f32 v[20:21], v[24:25], v[52:53], v[20:21] op_sel_hi:[1,0,1]
	v_mov_b32_e32 v30, v23
	v_pk_fma_f32 v[96:97], v[30:31], v[76:77], v[20:21] op_sel_hi:[1,0,1]
	v_mov_b32_e32 v20, v12
	v_mov_b32_e32 v21, v16
	v_pk_fma_f32 v[14:15], v[20:21], v[26:27], v[14:15] op_sel_hi:[1,0,1]
	v_mov_b32_e32 v16, v13
	v_mov_b32_e32 v12, s68
	v_mov_b32_e32 v20, s67
	v_pk_fma_f32 v[16:17], v[16:17], v[90:91], v[14:15] op_sel_hi:[1,0,1]
	ds_read_b128 v[12:15], v12
	ds_read_b128 v[20:23], v20
	s_waitcnt lgkmcnt(1)
	v_mov_b32_e32 v24, v12
	s_waitcnt lgkmcnt(0)
	v_mov_b32_e32 v25, v20
	v_pk_fma_f32 v[16:17], v[24:25], v[42:43], v[16:17] op_sel_hi:[1,0,1]
	v_mov_b32_e32 v20, v13
	v_pk_fma_f32 v[12:13], v[20:21], v[84:85], v[16:17] op_sel_hi:[1,0,1]
	v_mov_b32_e32 v16, v14
	v_mov_b32_e32 v17, v22
	v_pk_fma_f32 v[12:13], v[16:17], v[54:55], v[12:13] op_sel_hi:[1,0,1]
	v_mov_b32_e32 v22, v15
	v_pk_fma_f32 v[16:17], v[22:23], v[86:87], v[12:13] op_sel_hi:[1,0,1]
	v_mov_b32_e32 v12, s66
	v_mov_b32_e32 v20, s65
	ds_read_b128 v[12:15], v12
	ds_read_b128 v[20:23], v20
	s_waitcnt lgkmcnt(1)
	v_mov_b32_e32 v24, v12
	s_waitcnt lgkmcnt(0)
	v_mov_b32_e32 v25, v20
	v_pk_fma_f32 v[16:17], v[24:25], v[50:51], v[16:17] op_sel_hi:[1,0,1]
	v_mov_b32_e32 v20, v13
	v_pk_fma_f32 v[12:13], v[20:21], v[82:83], v[16:17] op_sel_hi:[1,0,1]
	v_mov_b32_e32 v16, v14
	v_mov_b32_e32 v17, v22
	v_pk_fma_f32 v[12:13], v[16:17], v[52:53], v[12:13] op_sel_hi:[1,0,1]
	v_mov_b32_e32 v22, v15
	v_pk_fma_f32 v[98:99], v[22:23], v[76:77], v[12:13] op_sel_hi:[1,0,1]
	v_mov_b32_e32 v12, v4
	v_mov_b32_e32 v13, v8
	v_pk_fma_f32 v[6:7], v[12:13], v[26:27], v[6:7] op_sel_hi:[1,0,1]
	v_mov_b32_e32 v8, v5
	v_mov_b32_e32 v4, s29
	v_mov_b32_e32 v12, s28
	v_pk_fma_f32 v[8:9], v[8:9], v[90:91], v[6:7] op_sel_hi:[1,0,1]
	ds_read_b128 v[4:7], v4
	ds_read_b128 v[12:15], v12
	s_waitcnt lgkmcnt(1)
	v_mov_b32_e32 v16, v4
	s_waitcnt lgkmcnt(0)
	v_mov_b32_e32 v17, v12
	v_pk_fma_f32 v[8:9], v[16:17], v[42:43], v[8:9] op_sel_hi:[1,0,1]
	v_mov_b32_e32 v12, v5
	v_pk_fma_f32 v[4:5], v[12:13], v[84:85], v[8:9] op_sel_hi:[1,0,1]
	v_mov_b32_e32 v8, v6
	v_mov_b32_e32 v9, v14
	v_pk_fma_f32 v[4:5], v[8:9], v[54:55], v[4:5] op_sel_hi:[1,0,1]
	v_mov_b32_e32 v14, v7
	v_pk_fma_f32 v[8:9], v[14:15], v[86:87], v[4:5] op_sel_hi:[1,0,1]
	v_mov_b32_e32 v4, s5
	v_mov_b32_e32 v12, s4
	ds_read_b128 v[4:7], v4
	ds_read_b128 v[12:15], v12
	s_add_i32 s4, s27, 0x1883c
	s_add_i32 s27, s27, 64
	s_cmp_lt_i32 s26, s30
	s_waitcnt lgkmcnt(1)
	v_mov_b32_e32 v16, v4
	s_waitcnt lgkmcnt(0)
	v_mov_b32_e32 v17, v12
	v_pk_fma_f32 v[8:9], v[16:17], v[50:51], v[8:9] op_sel_hi:[1,0,1]
	v_mov_b32_e32 v12, v5
	v_pk_fma_f32 v[4:5], v[12:13], v[82:83], v[8:9] op_sel_hi:[1,0,1]
	v_mov_b32_e32 v8, v6
	v_mov_b32_e32 v9, v14
	v_pk_fma_f32 v[4:5], v[8:9], v[52:53], v[4:5] op_sel_hi:[1,0,1]
	v_mov_b32_e32 v14, v7
	v_pk_fma_f32 v[94:95], v[14:15], v[76:77], v[4:5] op_sel_hi:[1,0,1]
	v_mov_b32_e32 v4, s4
	ds_read_b32 v4, v4
	s_waitcnt lgkmcnt(0)
	v_fmac_f32_e32 v109, v4, v76
	s_cbranch_scc1 .LBB0_17
	v_add_u32_e32 v4, s31, v75
	ds_write2st64_b32 v4, v2, v3 offset1:1
	ds_write2st64_b32 v4, v10, v11 offset0:2 offset1:3
	ds_write2st64_b32 v4, v18, v19 offset0:4 offset1:5
	ds_write2st64_b32 v4, v34, v35 offset0:6 offset1:7
	ds_write2st64_b32 v4, v92, v93 offset0:8 offset1:9
	ds_write2st64_b32 v4, v96, v97 offset0:10 offset1:11
	ds_write2st64_b32 v4, v98, v99 offset0:12 offset1:13
	ds_write2st64_b32 v4, v94, v95 offset0:14 offset1:15
	ds_write_b32 v4, v109 offset:4096
	s_waitcnt lgkmcnt(0)
	s_barrier
	s_and_saveexec_b64 s[26:27], vcc
	s_cbranch_execz .LBB0_15
	s_mul_i32 s4, s11, 0x1800
	s_add_i32 s4, s4, s10
	v_or_b32_e32 v2, s4, v1
	s_mul_hi_i32 s29, s11, 17
	s_mul_i32 s28, s11, 17
	s_ashr_i32 s11, s10, 31
	v_ashrrev_i32_e32 v3, 31, v2
	v_lshl_add_u64 v[2:3], v[2:3], 2, s[8:9]
	v_lshl_add_u64 v[4:5], s[10:11], 2, v[78:79]
	s_mov_b64 s[10:11], 0
	v_mov_b32_e32 v6, v74
